# MoE GEMM set-up and combine expert-offset tables built by a 32-lane DPP scan (one count load per lane) instead of thread 0's serial batches
# speedup vs baseline: 1.0066x; 1.0066x over previous
; #define LAS __attribute__((address_space(3)))
; __device__ __forceinline__ int tid_hidden() { int t = threadIdx.x; asm volatile("" : "+v"(t)); return t; }
; #define lds lds_hidden(lds0)
;     __device__ __forceinline__ void init(LAS unsigned char* lds, const bf16_t* A_, const int* ltok_, const bf16_t* Bt_, const int* cnt, int G, int c) {
;         A = A_; ltok = ltok_; Bt = Bt_;
;         LAS int* t = (LAS int*)(lds + PRE_OFF); tb = t;
;         __syncthreads();
;         const int tidi = tid_hidden();
;         if (tidi == 0) { int run = 0, ro = 0; for (int e = 0; e < NE; ++e) { const int ce = cnt[e]; t[e] = run; t[33 + e] = ro; t[66 + e] = ce; run += ((ce + 255) >> 8) * NTN; ro += ((ce + 255) >> 8) << 8;   } t[32] = run; t[65] = ro; }
;         __syncthreads();
.LBB0_1341:
	s_cmp_le_i32 s81, s26
	s_cselect_b64 s[0:1], -1, 0
	s_cmp_lt_i32 s26, s82
	s_cselect_b64 s[2:3], -1, 0
	s_and_b64 s[0:1], s[0:1], s[2:3]
	s_andn2_b64 vcc, exec, s[0:1]
	s_cbranch_vccnz .LBB0_1424
	s_mov_b32 s66, s91
	s_mov_b64 s[0:1], s[86:87]
	s_load_dwordx2 s[0:1], s[0:1], 0xa8
	s_mov_b64 s[2:3], s[86:87]
	v_readlane_b32 s7, v254, 0
	s_waitcnt vmcnt(0)
	v_mov_b32_e32 v20, v0
	s_waitcnt lgkmcnt(0)
	s_add_u32 s8, s0, 0x8008000
	s_addc_u32 s9, s1, 0
	s_load_dwordx2 s[0:1], s[2:3], 0xa8
	s_mov_b64 s[2:3], s[86:87]
	s_waitcnt lgkmcnt(0)
	s_add_u32 s10, s0, 0x1bf4d000
	s_addc_u32 s11, s1, 0
	s_load_dwordx2 s[0:1], s[2:3], 0xa8
	s_mov_b64 s[2:3], s[86:87]
	s_waitcnt lgkmcnt(0)
	s_add_u32 s0, s0, 0x305cd000
	s_addc_u32 s1, s1, 0
	s_load_dwordx2 s[2:3], s[2:3], 0xa8
	s_waitcnt lgkmcnt(0)
	s_add_u32 s4, s2, 0x3600
	s_addc_u32 s5, s3, 0
	s_load_dword s6, s[78:79], 0x0
	s_add_i32 s31, s66, 0x20800
	s_waitcnt lgkmcnt(0)
	s_barrier
	s_nop 0
	v_cmp_gt_u32_e32 vcc, 32, v20
	s_and_saveexec_b64 s[2:3], vcc
	s_cbranch_execz .LBB0_1344
	s_lshl_b32 s90, s40, 5
	s_lshl_b64 s[12:13], s[90:91], 2
	s_add_u32 s4, s4, s12
	s_addc_u32 s5, s5, s13
	v_lshlrev_b32_e32 v2, 2, v20
	global_load_dword v3, v2, s[4:5]
	s_add_i32 s12, s66, 0x20800
	v_add_u32_e32 v9, s12, v2
	v_cmp_lt_u32_e32 vcc, 15, v20
	s_waitcnt vmcnt(0)
	v_add_u32_e32 v4, 0xff, v3
	v_lshrrev_b32_e32 v4, 8, v4
	v_mov_b32_e32 v5, v4
	s_nop 1
	v_add_u32_dpp v5, v5, v5 row_shr:1 row_mask:0xf bank_mask:0xf bound_ctrl:0
	s_nop 1
	v_add_u32_dpp v5, v5, v5 row_shr:2 row_mask:0xf bank_mask:0xf bound_ctrl:0
	s_nop 1
	v_add_u32_dpp v5, v5, v5 row_shr:4 row_mask:0xf bank_mask:0xf bound_ctrl:0
	s_nop 1
	v_add_u32_dpp v5, v5, v5 row_shr:8 row_mask:0xf bank_mask:0xf bound_ctrl:0
	s_nop 1
	v_readlane_b32 s13, v5, 15
	s_nop 3
	v_mov_b32_e32 v6, s13
	v_cndmask_b32_e32 v6, v35, v6, vcc
	v_add_u32_e32 v5, v5, v6
	v_sub_u32_e32 v7, v5, v4
	v_lshlrev_b32_e32 v8, 3, v7
	v_lshlrev_b32_e32 v10, 8, v7
	ds_write_b32 v9, v8
	ds_write_b32 v9, v10 offset:132
	ds_write_b32 v9, v3 offset:264
	v_lshlrev_b32_e32 v8, 3, v5
	v_lshlrev_b32_e32 v10, 8, v5
	v_cmp_eq_u32_e32 vcc, 31, v20
	s_and_b64 exec, exec, vcc
	ds_write_b32 v9, v8 offset:4
	ds_write_b32 v9, v10 offset:136

; #define LAS __attribute__((address_space(3)))
; __device__ __forceinline__ int tid_hidden() { int t = threadIdx.x; asm volatile("" : "+v"(t)); return t; }
; #define lds lds_hidden(lds0)
;     __device__ __forceinline__ void init(LAS unsigned char* lds, const bf16_t* A_, const int* ltok_, const bf16_t* Bt_, const int* cnt, int G, int c) {
;         A = A_; ltok = ltok_; Bt = Bt_;
;         LAS int* t = (LAS int*)(lds + PRE_OFF); tb = t;
;         __syncthreads();
;         const int tidi = tid_hidden();
;         if (tidi == 0) { int run = 0, ro = 0; for (int e = 0; e < NE; ++e) { const int ce = cnt[e]; t[e] = run; t[33 + e] = ro; t[66 + e] = ce; run += ((ce + 255) >> 8) * NTN; ro += ((ce + 255) >> 8) << 8;   } t[32] = run; t[65] = ro; }
;         __syncthreads();
.LBB0_1386:
	s_mov_b32 s61, s91
	s_mov_b64 s[0:1], s[86:87]
	s_load_dwordx2 s[0:1], s[0:1], 0xa8
	s_mov_b64 s[2:3], s[86:87]
	v_readlane_b32 s11, v254, 0
	v_mov_b32_e32 v20, v0
	s_waitcnt lgkmcnt(0)
	s_add_u32 s4, s0, 0x1c3cd000
	s_addc_u32 s5, s1, 0
	s_load_dwordx2 s[0:1], s[2:3], 0xa8
	s_mov_b64 s[2:3], s[86:87]
	s_waitcnt lgkmcnt(0)
	s_add_u32 s0, s0, 0x505cd000
	s_addc_u32 s1, s1, 0
	s_load_dwordx2 s[2:3], s[2:3], 0xa8
	s_waitcnt lgkmcnt(0)
	s_add_u32 s8, s2, 0x3600
	s_addc_u32 s9, s3, 0
	s_load_dword s10, s[78:79], 0x0
	s_add_i32 s30, s61, 0x20800
	s_waitcnt lgkmcnt(0)
	s_waitcnt vmcnt(0)
	s_barrier
	s_nop 0
	v_cmp_gt_u32_e32 vcc, 32, v20
	s_and_saveexec_b64 s[2:3], vcc
	s_cbranch_execz .LBB0_1388
	s_lshl_b32 s90, s40, 5
	s_lshl_b64 s[12:13], s[90:91], 2
	s_add_u32 s8, s8, s12
	s_addc_u32 s9, s9, s13
	v_lshlrev_b32_e32 v2, 2, v20
	global_load_dword v3, v2, s[8:9]
	s_add_i32 s12, s61, 0x20800
	v_add_u32_e32 v9, s12, v2
	v_cmp_lt_u32_e32 vcc, 15, v20
	s_waitcnt vmcnt(0)
	v_add_u32_e32 v4, 0xff, v3
	v_lshrrev_b32_e32 v4, 8, v4
	v_mov_b32_e32 v5, v4
	s_nop 1
	v_add_u32_dpp v5, v5, v5 row_shr:1 row_mask:0xf bank_mask:0xf bound_ctrl:0
	s_nop 1
	v_add_u32_dpp v5, v5, v5 row_shr:2 row_mask:0xf bank_mask:0xf bound_ctrl:0
	s_nop 1
	v_add_u32_dpp v5, v5, v5 row_shr:4 row_mask:0xf bank_mask:0xf bound_ctrl:0
	s_nop 1
	v_add_u32_dpp v5, v5, v5 row_shr:8 row_mask:0xf bank_mask:0xf bound_ctrl:0
	s_nop 1
	v_readlane_b32 s13, v5, 15
	s_nop 3
	v_mov_b32_e32 v6, s13
	v_cndmask_b32_e32 v6, v35, v6, vcc
	v_add_u32_e32 v5, v5, v6
	v_sub_u32_e32 v7, v5, v4
	v_lshlrev_b32_e32 v8, 2, v7
	v_lshlrev_b32_e32 v10, 8, v7
	ds_write_b32 v9, v8
	ds_write_b32 v9, v10 offset:132
	ds_write_b32 v9, v3 offset:264
	v_lshlrev_b32_e32 v8, 2, v5
	v_lshlrev_b32_e32 v10, 8, v5
	v_cmp_eq_u32_e32 vcc, 31, v20
	s_and_b64 exec, exec, vcc
	ds_write_b32 v9, v8 offset:4
	ds_write_b32 v9, v10 offset:136

; #define LAS __attribute__((address_space(3)))
; __device__ __forceinline__ int tid_hidden() { int t = threadIdx.x; asm volatile("" : "+v"(t)); return t; }
; #define lds lds_hidden(lds0)
; __device__ __forceinline__ void combine_phase(LAS unsigned char* lds, const bf16_t* X, bf16_t* Xo, const unsigned char* __restrict__ YB, const float* __restrict__ mod_l, const int* __restrict__ cnt_l, ...
;     const int tid = tid_hidden(), wid = tid >> 6, lane = tid & 63;
;     LAS int* offp = (LAS int*)lds;
;     __syncthreads();
;     if (tid == 0) { int run = 0; for (int e = 0; e < NE; ++e) { offp[e] = run; run += ((cnt_l[e] + 255) >> 8) << 8; } }
;     __syncthreads();
.LBB0_1490:
	s_mov_b64 s[16:17], s[86:87]
	s_load_dwordx2 s[16:17], s[16:17], 0xa8
	s_mov_b64 s[24:25], s[86:87]
	v_readlane_b32 s30, v254, 0
	s_waitcnt vmcnt(0)
	v_mov_b32_e32 v18, v0
	s_waitcnt lgkmcnt(0)
	s_add_u32 s22, s16, 0x4008000
	s_addc_u32 s23, s17, 0
	s_load_dwordx2 s[24:25], s[24:25], 0xa0
	s_nop 0
	s_load_dword s29, s[78:79], 0x0
	s_waitcnt lgkmcnt(0)
	s_nop 0
	v_cmp_gt_u32_e32 vcc, 32, v18
	s_barrier
	s_and_saveexec_b64 s[16:17], vcc
	s_cbranch_execz .LBB0_1492
	s_lshl_b32 s34, s40, 5
	s_mov_b32 s35, s91
	s_lshl_b64 s[34:35], s[34:35], 2
	s_add_u32 s26, s26, s34
	s_addc_u32 s27, s27, s35
	v_lshlrev_b32_e32 v2, 2, v18
	global_load_dword v3, v2, s[26:27]
	v_add_u32_e32 v9, s28, v2
	v_cmp_lt_u32_e32 vcc, 15, v18
	s_waitcnt vmcnt(0)
	v_add_u32_e32 v4, 0xff, v3
	v_and_b32_e32 v4, 0xffffff00, v4
	v_mov_b32_e32 v5, v4
	s_nop 1
	v_add_u32_dpp v5, v5, v5 row_shr:1 row_mask:0xf bank_mask:0xf bound_ctrl:0
	s_nop 1
	v_add_u32_dpp v5, v5, v5 row_shr:2 row_mask:0xf bank_mask:0xf bound_ctrl:0
	s_nop 1
	v_add_u32_dpp v5, v5, v5 row_shr:4 row_mask:0xf bank_mask:0xf bound_ctrl:0
	s_nop 1
	v_add_u32_dpp v5, v5, v5 row_shr:8 row_mask:0xf bank_mask:0xf bound_ctrl:0
	s_nop 1
	v_readlane_b32 s34, v5, 15
	s_nop 3
	v_mov_b32_e32 v6, s34
	v_cndmask_b32_e32 v6, v35, v6, vcc
	v_add_u32_e32 v5, v5, v6
	v_sub_u32_e32 v7, v5, v4
	ds_write_b32 v9, v7
